# hot loop heads (five GEMM K-loops, attention key loop) pinned to 64-byte boundaries with s_nop fill (on top of v33)
# baseline (speedup 1.0000x reference)
.LBB0_343:
	s_ashr_i32 s51, s50, 31
	v_mov_b64_e32 v[2:3], 0x77a
	s_lshl_b64 s[14:15], s[50:51], 19
	v_cmp_lt_i64_e32 vcc, s[52:53], v[2:3]
	s_add_u32 s52, s42, s14
	s_addc_u32 s53, s43, s15
	s_and_b64 s[14:15], vcc, exec
	s_cselect_b32 s9, s53, s57
	s_cselect_b32 s14, s52, s56
	s_ashr_i32 s49, s48, 31
	s_lshl_b64 s[54:55], s[48:49], 19
	s_add_u32 s54, s63, s54
	s_addc_u32 s55, s64, s55
	s_and_b64 s[58:59], vcc, exec
	s_cselect_b32 s15, s55, s39
	s_cselect_b32 s35, s54, s38
	s_add_u32 s37, s38, 0x100
	s_addc_u32 s49, s39, 0
	s_add_u32 s38, s56, 0x40080
	v_mov_b32_e32 v2, 0
	s_addc_u32 s39, s57, 0
	s_mov_b32 s51, -2
	v_mov_b32_e32 v3, v2
	v_mov_b32_e32 v4, v2
	v_mov_b32_e32 v5, v2
	v_mov_b32_e32 v6, v2
	v_mov_b32_e32 v7, v2
	v_mov_b32_e32 v8, v2
	v_mov_b32_e32 v9, v2
	v_mov_b32_e32 v10, v2
	v_mov_b32_e32 v11, v2
	v_mov_b32_e32 v12, v2
	v_mov_b32_e32 v13, v2
	v_mov_b32_e32 v14, v2
	v_mov_b32_e32 v15, v2
	v_mov_b32_e32 v16, v2
	v_mov_b32_e32 v17, v2
	v_mov_b32_e32 v18, v2
	v_mov_b32_e32 v19, v2
	v_mov_b32_e32 v20, v2
	v_mov_b32_e32 v21, v2
	v_mov_b32_e32 v22, v2
	v_mov_b32_e32 v23, v2
	v_mov_b32_e32 v24, v2
	v_mov_b32_e32 v25, v2
	v_mov_b32_e32 v26, v2
	v_mov_b32_e32 v27, v2
	v_mov_b32_e32 v28, v2
	v_mov_b32_e32 v29, v2
	v_mov_b32_e32 v30, v2
	v_mov_b32_e32 v31, v2
	v_mov_b32_e32 v32, v2
	v_mov_b32_e32 v33, v2
	v_mov_b32_e32 v66, v2
	v_mov_b32_e32 v67, v2
	v_mov_b32_e32 v68, v2
	v_mov_b32_e32 v69, v2
	v_mov_b32_e32 v70, v2
	v_mov_b32_e32 v71, v2
	v_mov_b32_e32 v72, v2
	v_mov_b32_e32 v73, v2
	v_mov_b32_e32 v74, v2
	v_mov_b32_e32 v75, v2
	v_mov_b32_e32 v76, v2
	v_mov_b32_e32 v77, v2
	v_mov_b32_e32 v78, v2
	v_mov_b32_e32 v79, v2
	v_mov_b32_e32 v80, v2
	v_mov_b32_e32 v81, v2
	v_mov_b32_e32 v82, v2
	v_mov_b32_e32 v83, v2
	v_mov_b32_e32 v84, v2
	v_mov_b32_e32 v85, v2
	v_mov_b32_e32 v86, v2
	v_mov_b32_e32 v87, v2
	v_mov_b32_e32 v88, v2
	v_mov_b32_e32 v89, v2
	v_mov_b32_e32 v90, v2
	v_mov_b32_e32 v91, v2
	v_mov_b32_e32 v92, v2
	v_mov_b32_e32 v93, v2
	v_mov_b32_e32 v94, v2
	v_mov_b32_e32 v95, v2
	v_mov_b32_e32 v96, v2
	v_mov_b32_e32 v97, v2
	v_mov_b32_e32 v34, v2
	v_mov_b32_e32 v35, v2
	v_mov_b32_e32 v36, v2
	v_mov_b32_e32 v37, v2
	v_mov_b32_e32 v38, v2
	v_mov_b32_e32 v39, v2
	v_mov_b32_e32 v40, v2
	v_mov_b32_e32 v41, v2
	v_mov_b32_e32 v42, v2
	v_mov_b32_e32 v43, v2
	v_mov_b32_e32 v44, v2
	v_mov_b32_e32 v45, v2
	v_mov_b32_e32 v46, v2
	v_mov_b32_e32 v47, v2
	v_mov_b32_e32 v48, v2
	v_mov_b32_e32 v49, v2
	v_mov_b32_e32 v50, v2
	v_mov_b32_e32 v51, v2
	v_mov_b32_e32 v52, v2
	v_mov_b32_e32 v53, v2
	v_mov_b32_e32 v54, v2
	v_mov_b32_e32 v55, v2
	v_mov_b32_e32 v56, v2
	v_mov_b32_e32 v57, v2
	v_mov_b32_e32 v58, v2
	v_mov_b32_e32 v59, v2
	v_mov_b32_e32 v60, v2
	v_mov_b32_e32 v61, v2
	v_mov_b32_e32 v62, v2
	v_mov_b32_e32 v63, v2
	v_mov_b32_e32 v64, v2
	v_mov_b32_e32 v65, v2
	v_mov_b32_e32 v98, v2
	v_mov_b32_e32 v99, v2
	v_mov_b32_e32 v100, v2
	v_mov_b32_e32 v101, v2
	v_mov_b32_e32 v102, v2
	v_mov_b32_e32 v103, v2
	v_mov_b32_e32 v104, v2
	v_mov_b32_e32 v105, v2
	v_mov_b32_e32 v106, v2
	v_mov_b32_e32 v107, v2
	v_mov_b32_e32 v108, v2
	v_mov_b32_e32 v109, v2
	v_mov_b32_e32 v110, v2
	v_mov_b32_e32 v111, v2
	v_mov_b32_e32 v112, v2
	v_mov_b32_e32 v113, v2
	v_mov_b32_e32 v114, v2
	v_mov_b32_e32 v115, v2
	v_mov_b32_e32 v116, v2
	v_mov_b32_e32 v117, v2
	v_mov_b32_e32 v118, v2
	v_mov_b32_e32 v119, v2
	v_mov_b32_e32 v120, v2
	v_mov_b32_e32 v121, v2
	v_mov_b32_e32 v122, v2
	v_mov_b32_e32 v123, v2
	v_mov_b32_e32 v124, v2
	v_mov_b32_e32 v125, v2
	v_mov_b32_e32 v126, v2
	v_mov_b32_e32 v127, v2
	v_mov_b32_e32 v128, v2
	v_mov_b32_e32 v129, v2
	s_lshl_b32 s96, s34, 8
	s_or_b32 s96, s96, s82
	v_or_b32_e32 v252, s96, v155
	v_add_u32_e32 v253, 0x80, v252
	v_min_u32_e32 v252, 0x1cb8, v252
	v_min_u32_e32 v253, 0x1cb8, v253
	v_lshlrev_b32_e32 v252, 2, v252
	v_lshlrev_b32_e32 v253, 2, v253
	global_load_dwordx4 v[240:243], v252, s[30:31]
	global_load_dwordx4 v[244:247], v252, s[30:31] offset:16
	global_load_dwordx4 v[248:251], v253, s[30:31]
	global_load_dwordx4 v[222:225], v253, s[30:31] offset:16
	.p2alignl 6, 3212836864

.LBB0_754:
	s_or_b64 exec, exec, s[14:15]
	s_waitcnt vmcnt(17)
	v_mad_u64_u32 v[106:107], s[14:15], v13, s8, v[14:15]
	v_mul_lo_u32 v20, v20, s25
	v_lshl_add_u32 v21, v106, 1, 0
	s_waitcnt vmcnt(1)
	ds_write_b128 v21, v[6:9] offset:64
	v_lshl_add_u32 v6, v128, 1, 0
	v_add_u32_e32 v129, v194, v20
	s_waitcnt vmcnt(0)
	ds_write_b128 v6, v[2:5] offset:64
	s_and_saveexec_b64 s[14:15], s[36:37]
	s_xor_b64 s[14:15], exec, s[14:15]
	v_add_u32_e32 v129, v194, v20
	s_andn2_saveexec_b64 s[14:15], s[14:15]
	v_lshl_add_u32 v2, v129, 1, 0
	ds_write_b128 v2, v[90:93] offset:13376
	s_or_b64 exec, exec, s[14:15]
	v_mad_i64_i32 v[2:3], s[14:15], v13, s24, 0
	s_add_i32 s70, s67, s68
	s_lshl_b64 s[14:15], s[70:71], 1
	s_add_u32 s14, s34, s14
	v_lshl_add_u64 v[4:5], v[194:195], 1, v[16:17]
	s_addc_u32 s15, s35, s15
	v_lshl_add_u64 v[4:5], s[14:15], 0, v[4:5]
	v_mad_u64_u32 v[2:3], s[14:15], s9, v229, v[2:3]
	v_mad_u64_u32 v[2:3], s[14:15], s66, v230, v[2:3]
	v_lshl_add_u64 v[2:3], v[14:15], 1, v[2:3]
	v_lshlrev_b32_e32 v194, 1, v12
	v_lshl_add_u64 v[2:3], s[42:43], 0, v[2:3]
	v_mov_b32_e32 v105, 0
	v_ashrrev_i32_e32 v103, 31, v102
	v_lshlrev_b32_e32 v104, 3, v19
	v_mul_u32_u24_e32 v130, 0x68, v18
	v_mul_u32_u24_e32 v107, 0x48, v18
	s_mov_b32 s30, 1
	v_lshl_add_u64 v[108:109], v[4:5], 0, s[10:11]
	v_lshl_add_u64 v[110:111], v[10:11], 0, v[194:195]
	v_lshl_add_u64 v[112:113], v[2:3], 0, s[12:13]
	v_mov_b32_e32 v18, 0
	v_mov_b32_e32 v19, v105
	v_mov_b32_e32 v20, v105
	v_mov_b32_e32 v21, v105
	v_mov_b32_e32 v22, v105
	v_mov_b32_e32 v23, v105
	v_mov_b32_e32 v24, v105
	v_mov_b32_e32 v25, v105
	v_mov_b32_e32 v26, v105
	v_mov_b32_e32 v27, v105
	v_mov_b32_e32 v28, v105
	v_mov_b32_e32 v29, v105
	v_mov_b32_e32 v30, v105
	v_mov_b32_e32 v31, v105
	v_mov_b32_e32 v32, v105
	v_mov_b32_e32 v33, v105
	v_mov_b32_e32 v2, 0
	v_mov_b32_e32 v3, v105
	v_mov_b32_e32 v4, v105
	v_mov_b32_e32 v5, v105
	v_mov_b32_e32 v6, v105
	v_mov_b32_e32 v7, v105
	v_mov_b32_e32 v8, v105
	v_mov_b32_e32 v9, v105
	v_mov_b32_e32 v10, v105
	v_mov_b32_e32 v11, v105
	v_mov_b32_e32 v12, v105
	v_mov_b32_e32 v13, v105
	v_mov_b32_e32 v14, v105
	v_mov_b32_e32 v15, v105
	v_mov_b32_e32 v16, v105
	v_mov_b32_e32 v17, v105
	s_waitcnt lgkmcnt(0)
	s_barrier
	s_cmp_lg_u64 vcc, 0
	s_cselect_b32 s43, 1, 0
	v_add_lshl_u32 v130, v130, v104, 1
	v_add_lshl_u32 v107, v107, v104, 1
	v_lshlrev_b32_e32 v106, 1, v106
	v_lshlrev_b32_e32 v128, 1, v128
	v_lshlrev_b32_e32 v129, 1, v129
	v_mov_b32_e32 v145, 0
	v_mov_b32_e32 v50, 0
	v_mov_b32_e32 v51, 0
	v_mov_b32_e32 v52, 0
	v_mov_b32_e32 v53, 0
	v_mov_b32_e32 v54, 0
	v_mov_b32_e32 v55, 0
	v_mov_b32_e32 v56, 0
	v_mov_b32_e32 v57, 0
	v_mov_b32_e32 v58, 0
	v_mov_b32_e32 v59, 0
	v_mov_b32_e32 v60, 0
	v_mov_b32_e32 v61, 0
	v_mov_b32_e32 v62, 0
	v_mov_b32_e32 v63, 0
	v_mov_b32_e32 v64, 0
	v_mov_b32_e32 v65, 0
	s_mov_b32 s30, 0
	.p2alignl 6, 3212836864

.LBB0_1079:
	s_ashr_i32 s1, s0, 31
	s_lshl_b64 s[14:15], s[0:1], 18
	s_add_u32 s44, s30, s14
	s_addc_u32 s45, s31, s15
	s_and_b64 s[14:15], s[56:57], exec
	s_cselect_b32 s1, s45, s55
	s_cselect_b32 s14, s44, s54
	s_ashr_i32 s35, s34, 31
	s_lshl_b64 s[46:47], s[34:35], 18
	s_add_u32 s46, s60, s46
	s_addc_u32 s47, s61, s47
	s_and_b64 s[56:57], s[56:57], exec
	s_cselect_b32 s15, s47, s53
	s_cselect_b32 s35, s46, s52
	s_add_u32 s69, s52, 0x100
	s_addc_u32 s70, s53, 0
	s_add_u32 s52, s54, 0x20080
	v_mov_b32_e32 v2, 0
	s_addc_u32 s53, s55, 0
	s_mov_b32 s82, -2
	v_mov_b32_e32 v3, v2
	v_mov_b32_e32 v4, v2
	v_mov_b32_e32 v5, v2
	v_mov_b32_e32 v6, v2
	v_mov_b32_e32 v7, v2
	v_mov_b32_e32 v8, v2
	v_mov_b32_e32 v9, v2
	v_mov_b32_e32 v10, v2
	v_mov_b32_e32 v11, v2
	v_mov_b32_e32 v12, v2
	v_mov_b32_e32 v13, v2
	v_mov_b32_e32 v18, v2
	v_mov_b32_e32 v19, v2
	v_mov_b32_e32 v20, v2
	v_mov_b32_e32 v21, v2
	v_mov_b32_e32 v26, v2
	v_mov_b32_e32 v27, v2
	v_mov_b32_e32 v28, v2
	v_mov_b32_e32 v29, v2
	v_mov_b32_e32 v34, v2
	v_mov_b32_e32 v35, v2
	v_mov_b32_e32 v36, v2
	v_mov_b32_e32 v37, v2
	v_mov_b32_e32 v42, v2
	v_mov_b32_e32 v43, v2
	v_mov_b32_e32 v44, v2
	v_mov_b32_e32 v45, v2
	v_mov_b32_e32 v50, v2
	v_mov_b32_e32 v51, v2
	v_mov_b32_e32 v52, v2
	v_mov_b32_e32 v53, v2
	v_mov_b32_e32 v14, v2
	v_mov_b32_e32 v15, v2
	v_mov_b32_e32 v16, v2
	v_mov_b32_e32 v17, v2
	v_mov_b32_e32 v22, v2
	v_mov_b32_e32 v23, v2
	v_mov_b32_e32 v24, v2
	v_mov_b32_e32 v25, v2
	v_mov_b32_e32 v30, v2
	v_mov_b32_e32 v31, v2
	v_mov_b32_e32 v32, v2
	v_mov_b32_e32 v33, v2
	v_mov_b32_e32 v38, v2
	v_mov_b32_e32 v39, v2
	v_mov_b32_e32 v40, v2
	v_mov_b32_e32 v41, v2
	v_mov_b32_e32 v46, v2
	v_mov_b32_e32 v47, v2
	v_mov_b32_e32 v48, v2
	v_mov_b32_e32 v49, v2
	v_mov_b32_e32 v54, v2
	v_mov_b32_e32 v55, v2
	v_mov_b32_e32 v56, v2
	v_mov_b32_e32 v57, v2
	v_mov_b32_e32 v58, v2
	v_mov_b32_e32 v59, v2
	v_mov_b32_e32 v60, v2
	v_mov_b32_e32 v61, v2
	v_mov_b32_e32 v62, v2
	v_mov_b32_e32 v63, v2
	v_mov_b32_e32 v64, v2
	v_mov_b32_e32 v65, v2
	v_mov_b32_e32 v66, v2
	v_mov_b32_e32 v67, v2
	v_mov_b32_e32 v68, v2
	v_mov_b32_e32 v69, v2
	v_mov_b32_e32 v70, v2
	v_mov_b32_e32 v71, v2
	v_mov_b32_e32 v72, v2
	v_mov_b32_e32 v73, v2
	v_mov_b32_e32 v74, v2
	v_mov_b32_e32 v75, v2
	v_mov_b32_e32 v76, v2
	v_mov_b32_e32 v77, v2
	v_mov_b32_e32 v82, v2
	v_mov_b32_e32 v83, v2
	v_mov_b32_e32 v84, v2
	v_mov_b32_e32 v85, v2
	v_mov_b32_e32 v90, v2
	v_mov_b32_e32 v91, v2
	v_mov_b32_e32 v92, v2
	v_mov_b32_e32 v93, v2
	v_mov_b32_e32 v98, v2
	v_mov_b32_e32 v99, v2
	v_mov_b32_e32 v100, v2
	v_mov_b32_e32 v101, v2
	v_mov_b32_e32 v106, v2
	v_mov_b32_e32 v107, v2
	v_mov_b32_e32 v108, v2
	v_mov_b32_e32 v109, v2
	v_mov_b32_e32 v114, v2
	v_mov_b32_e32 v115, v2
	v_mov_b32_e32 v116, v2
	v_mov_b32_e32 v117, v2
	v_mov_b32_e32 v78, v2
	v_mov_b32_e32 v79, v2
	v_mov_b32_e32 v80, v2
	v_mov_b32_e32 v81, v2
	v_mov_b32_e32 v86, v2
	v_mov_b32_e32 v87, v2
	v_mov_b32_e32 v88, v2
	v_mov_b32_e32 v89, v2
	v_mov_b32_e32 v94, v2
	v_mov_b32_e32 v95, v2
	v_mov_b32_e32 v96, v2
	v_mov_b32_e32 v97, v2
	v_mov_b32_e32 v102, v2
	v_mov_b32_e32 v103, v2
	v_mov_b32_e32 v104, v2
	v_mov_b32_e32 v105, v2
	v_mov_b32_e32 v110, v2
	v_mov_b32_e32 v111, v2
	v_mov_b32_e32 v112, v2
	v_mov_b32_e32 v113, v2
	v_mov_b32_e32 v118, v2
	v_mov_b32_e32 v119, v2
	v_mov_b32_e32 v120, v2
	v_mov_b32_e32 v121, v2
	v_mov_b32_e32 v122, v2
	v_mov_b32_e32 v123, v2
	v_mov_b32_e32 v124, v2
	v_mov_b32_e32 v125, v2
	v_mov_b32_e32 v126, v2
	v_mov_b32_e32 v127, v2
	v_mov_b32_e32 v128, v2
	v_mov_b32_e32 v129, v2
	.p2alignl 6, 3212836864

.LBB0_1255:
	s_ashr_i32 s49, s48, 31
	v_mov_b64_e32 v[2:3], 0x100
	s_lshl_b64 s[14:15], s[48:49], 19
	v_cmp_lt_i64_e32 vcc, s[50:51], v[2:3]
	s_add_u32 s50, s40, s14
	s_addc_u32 s51, s41, s15
	s_and_b64 s[14:15], vcc, exec
	s_cselect_b32 s14, s51, s57
	s_cselect_b32 s15, s50, s56
	s_ashr_i32 s35, s34, 31
	s_lshl_b64 s[52:53], s[34:35], 19
	s_add_u32 s52, s60, s52
	s_addc_u32 s53, s61, s53
	s_and_b64 s[58:59], vcc, exec
	s_cselect_b32 s35, s53, s55
	s_cselect_b32 s49, s52, s54
	s_add_u32 s86, s54, 0x100
	s_addc_u32 s87, s55, 0
	s_add_u32 s54, s56, 0x40080
	v_mov_b32_e32 v2, 0
	s_addc_u32 s55, s57, 0
	s_mov_b32 vcc_lo, -2
	v_mov_b32_e32 v3, v2
	v_mov_b32_e32 v4, v2
	v_mov_b32_e32 v5, v2
	v_mov_b32_e32 v6, v2
	v_mov_b32_e32 v7, v2
	v_mov_b32_e32 v8, v2
	v_mov_b32_e32 v9, v2
	v_mov_b32_e32 v14, v2
	v_mov_b32_e32 v15, v2
	v_mov_b32_e32 v16, v2
	v_mov_b32_e32 v17, v2
	v_mov_b32_e32 v22, v2
	v_mov_b32_e32 v23, v2
	v_mov_b32_e32 v24, v2
	v_mov_b32_e32 v25, v2
	v_mov_b32_e32 v30, v2
	v_mov_b32_e32 v31, v2
	v_mov_b32_e32 v32, v2
	v_mov_b32_e32 v33, v2
	v_mov_b32_e32 v34, v2
	v_mov_b32_e32 v35, v2
	v_mov_b32_e32 v36, v2
	v_mov_b32_e32 v37, v2
	v_mov_b32_e32 v46, v2
	v_mov_b32_e32 v47, v2
	v_mov_b32_e32 v48, v2
	v_mov_b32_e32 v49, v2
	v_mov_b32_e32 v50, v2
	v_mov_b32_e32 v51, v2
	v_mov_b32_e32 v52, v2
	v_mov_b32_e32 v53, v2
	v_mov_b32_e32 v10, v2
	v_mov_b32_e32 v11, v2
	v_mov_b32_e32 v12, v2
	v_mov_b32_e32 v13, v2
	v_mov_b32_e32 v18, v2
	v_mov_b32_e32 v19, v2
	v_mov_b32_e32 v20, v2
	v_mov_b32_e32 v21, v2
	v_mov_b32_e32 v26, v2
	v_mov_b32_e32 v27, v2
	v_mov_b32_e32 v28, v2
	v_mov_b32_e32 v29, v2
	v_mov_b32_e32 v38, v2
	v_mov_b32_e32 v39, v2
	v_mov_b32_e32 v40, v2
	v_mov_b32_e32 v41, v2
	v_mov_b32_e32 v42, v2
	v_mov_b32_e32 v43, v2
	v_mov_b32_e32 v44, v2
	v_mov_b32_e32 v45, v2
	v_mov_b32_e32 v54, v2
	v_mov_b32_e32 v55, v2
	v_mov_b32_e32 v56, v2
	v_mov_b32_e32 v57, v2
	v_mov_b32_e32 v58, v2
	v_mov_b32_e32 v59, v2
	v_mov_b32_e32 v60, v2
	v_mov_b32_e32 v61, v2
	v_mov_b32_e32 v62, v2
	v_mov_b32_e32 v63, v2
	v_mov_b32_e32 v64, v2
	v_mov_b32_e32 v65, v2
	v_mov_b32_e32 v66, v2
	v_mov_b32_e32 v67, v2
	v_mov_b32_e32 v68, v2
	v_mov_b32_e32 v69, v2
	v_mov_b32_e32 v70, v2
	v_mov_b32_e32 v71, v2
	v_mov_b32_e32 v72, v2
	v_mov_b32_e32 v73, v2
	v_mov_b32_e32 v74, v2
	v_mov_b32_e32 v75, v2
	v_mov_b32_e32 v76, v2
	v_mov_b32_e32 v77, v2
	v_mov_b32_e32 v86, v2
	v_mov_b32_e32 v87, v2
	v_mov_b32_e32 v88, v2
	v_mov_b32_e32 v89, v2
	v_mov_b32_e32 v94, v2
	v_mov_b32_e32 v95, v2
	v_mov_b32_e32 v96, v2
	v_mov_b32_e32 v97, v2
	v_mov_b32_e32 v98, v2
	v_mov_b32_e32 v99, v2
	v_mov_b32_e32 v100, v2
	v_mov_b32_e32 v101, v2
	v_mov_b32_e32 v126, v2
	v_mov_b32_e32 v127, v2
	v_mov_b32_e32 v128, v2
	v_mov_b32_e32 v129, v2
	v_mov_b32_e32 v130, v2
	v_mov_b32_e32 v131, v2
	v_mov_b32_e32 v132, v2
	v_mov_b32_e32 v133, v2
	v_mov_b32_e32 v78, v2
	v_mov_b32_e32 v79, v2
	v_mov_b32_e32 v80, v2
	v_mov_b32_e32 v81, v2
	v_mov_b32_e32 v82, v2
	v_mov_b32_e32 v83, v2
	v_mov_b32_e32 v84, v2
	v_mov_b32_e32 v85, v2
	v_mov_b32_e32 v90, v2
	v_mov_b32_e32 v91, v2
	v_mov_b32_e32 v92, v2
	v_mov_b32_e32 v93, v2
	v_mov_b32_e32 v102, v2
	v_mov_b32_e32 v103, v2
	v_mov_b32_e32 v104, v2
	v_mov_b32_e32 v105, v2
	v_mov_b32_e32 v110, v2
	v_mov_b32_e32 v111, v2
	v_mov_b32_e32 v112, v2
	v_mov_b32_e32 v113, v2
	v_mov_b32_e32 v134, v2
	v_mov_b32_e32 v135, v2
	v_mov_b32_e32 v136, v2
	v_mov_b32_e32 v137, v2
	v_mov_b32_e32 v138, v2
	v_mov_b32_e32 v139, v2
	v_mov_b32_e32 v140, v2
	v_mov_b32_e32 v141, v2
	v_mov_b32_e32 v142, v2
	v_mov_b32_e32 v143, v2
	v_mov_b32_e32 v144, v2
	v_mov_b32_e32 v145, v2
	.p2alignl 6, 3212836864

.LBB0_1632:
	s_ashr_i32 s49, s48, 31
	s_lshl_b64 s[14:15], s[48:49], 19
	s_add_u32 s52, s59, s14
	s_addc_u32 s53, s60, s15
	s_and_b64 s[14:15], s[38:39], exec
	s_cselect_b32 s14, s53, s35
	s_cselect_b32 s15, s52, s34
	v_mov_b32_e32 v139, v195
	v_mov_b32_e32 v141, v195
	s_add_u32 s49, s34, 0x100
	v_mov_b32_e32 v2, 0
	v_lshl_add_u64 v[142:143], s[46:47], 0, v[140:141]
	v_lshl_add_u64 v[144:145], s[46:47], 0, v[138:139]
	s_addc_u32 s84, s35, 0
	s_mov_b32 s85, -2
	s_mov_b64 s[34:35], 0
	v_mov_b32_e32 v3, v2
	v_mov_b32_e32 v4, v2
	v_mov_b32_e32 v5, v2
	v_mov_b32_e32 v10, v2
	v_mov_b32_e32 v11, v2
	v_mov_b32_e32 v12, v2
	v_mov_b32_e32 v13, v2
	v_mov_b32_e32 v18, v2
	v_mov_b32_e32 v19, v2
	v_mov_b32_e32 v20, v2
	v_mov_b32_e32 v21, v2
	v_mov_b32_e32 v26, v2
	v_mov_b32_e32 v27, v2
	v_mov_b32_e32 v28, v2
	v_mov_b32_e32 v29, v2
	v_mov_b32_e32 v34, v2
	v_mov_b32_e32 v35, v2
	v_mov_b32_e32 v36, v2
	v_mov_b32_e32 v37, v2
	v_mov_b32_e32 v42, v2
	v_mov_b32_e32 v43, v2
	v_mov_b32_e32 v44, v2
	v_mov_b32_e32 v45, v2
	v_mov_b32_e32 v50, v2
	v_mov_b32_e32 v51, v2
	v_mov_b32_e32 v52, v2
	v_mov_b32_e32 v53, v2
	v_mov_b32_e32 v58, v2
	v_mov_b32_e32 v59, v2
	v_mov_b32_e32 v60, v2
	v_mov_b32_e32 v61, v2
	v_mov_b32_e32 v6, v2
	v_mov_b32_e32 v7, v2
	v_mov_b32_e32 v8, v2
	v_mov_b32_e32 v9, v2
	v_mov_b32_e32 v14, v2
	v_mov_b32_e32 v15, v2
	v_mov_b32_e32 v16, v2
	v_mov_b32_e32 v17, v2
	v_mov_b32_e32 v22, v2
	v_mov_b32_e32 v23, v2
	v_mov_b32_e32 v24, v2
	v_mov_b32_e32 v25, v2
	v_mov_b32_e32 v30, v2
	v_mov_b32_e32 v31, v2
	v_mov_b32_e32 v32, v2
	v_mov_b32_e32 v33, v2
	v_mov_b32_e32 v38, v2
	v_mov_b32_e32 v39, v2
	v_mov_b32_e32 v40, v2
	v_mov_b32_e32 v41, v2
	v_mov_b32_e32 v46, v2
	v_mov_b32_e32 v47, v2
	v_mov_b32_e32 v48, v2
	v_mov_b32_e32 v49, v2
	v_mov_b32_e32 v54, v2
	v_mov_b32_e32 v55, v2
	v_mov_b32_e32 v56, v2
	v_mov_b32_e32 v57, v2
	v_mov_b32_e32 v62, v2
	v_mov_b32_e32 v63, v2
	v_mov_b32_e32 v64, v2
	v_mov_b32_e32 v65, v2
	v_mov_b32_e32 v66, v2
	v_mov_b32_e32 v67, v2
	v_mov_b32_e32 v68, v2
	v_mov_b32_e32 v69, v2
	v_mov_b32_e32 v74, v2
	v_mov_b32_e32 v75, v2
	v_mov_b32_e32 v76, v2
	v_mov_b32_e32 v77, v2
	v_mov_b32_e32 v82, v2
	v_mov_b32_e32 v83, v2
	v_mov_b32_e32 v84, v2
	v_mov_b32_e32 v85, v2
	v_mov_b32_e32 v90, v2
	v_mov_b32_e32 v91, v2
	v_mov_b32_e32 v92, v2
	v_mov_b32_e32 v93, v2
	v_mov_b32_e32 v98, v2
	v_mov_b32_e32 v99, v2
	v_mov_b32_e32 v100, v2
	v_mov_b32_e32 v101, v2
	v_mov_b32_e32 v106, v2
	v_mov_b32_e32 v107, v2
	v_mov_b32_e32 v108, v2
	v_mov_b32_e32 v109, v2
	v_mov_b32_e32 v114, v2
	v_mov_b32_e32 v115, v2
	v_mov_b32_e32 v116, v2
	v_mov_b32_e32 v117, v2
	v_mov_b32_e32 v122, v2
	v_mov_b32_e32 v123, v2
	v_mov_b32_e32 v124, v2
	v_mov_b32_e32 v125, v2
	v_mov_b32_e32 v70, v2
	v_mov_b32_e32 v71, v2
	v_mov_b32_e32 v72, v2
	v_mov_b32_e32 v73, v2
	v_mov_b32_e32 v78, v2
	v_mov_b32_e32 v79, v2
	v_mov_b32_e32 v80, v2
	v_mov_b32_e32 v81, v2
	v_mov_b32_e32 v86, v2
	v_mov_b32_e32 v87, v2
	v_mov_b32_e32 v88, v2
	v_mov_b32_e32 v89, v2
	v_mov_b32_e32 v94, v2
	v_mov_b32_e32 v95, v2
	v_mov_b32_e32 v96, v2
	v_mov_b32_e32 v97, v2
	v_mov_b32_e32 v102, v2
	v_mov_b32_e32 v103, v2
	v_mov_b32_e32 v104, v2
	v_mov_b32_e32 v105, v2
	v_mov_b32_e32 v110, v2
	v_mov_b32_e32 v111, v2
	v_mov_b32_e32 v112, v2
	v_mov_b32_e32 v113, v2
	v_mov_b32_e32 v118, v2
	v_mov_b32_e32 v119, v2
	v_mov_b32_e32 v120, v2
	v_mov_b32_e32 v121, v2
	v_mov_b32_e32 v126, v2
	v_mov_b32_e32 v127, v2
	v_mov_b32_e32 v128, v2
	v_mov_b32_e32 v129, v2
	.p2alignl 6, 3212836864

.LBB0_1840:
	s_ashr_i32 s31, s30, 31
	s_lshl_b64 s[14:15], s[30:31], 19
	s_add_u32 s48, s40, s14
	s_addc_u32 s49, s41, s15
	s_and_b64 s[14:15], s[58:59], exec
	s_cselect_b32 s9, s49, s57
	s_cselect_b32 s14, s48, s56
	s_ashr_i32 s35, s34, 31
	s_lshl_b64 s[50:51], s[34:35], 19
	s_add_u32 s50, s63, s50
	s_addc_u32 s51, s64, s51
	s_and_b64 s[58:59], s[58:59], exec
	s_cselect_b32 s15, s51, s55
	s_cselect_b32 s31, s50, s54
	s_add_u32 s35, s54, 0x100
	s_addc_u32 s86, s55, 0
	s_add_u32 s54, s56, 0x40080
	v_mov_b32_e32 v2, 0
	s_addc_u32 s55, s57, 0
	s_mov_b32 s87, -2
	v_mov_b32_e32 v3, v2
	v_mov_b32_e32 v4, v2
	v_mov_b32_e32 v5, v2
	v_mov_b32_e32 v6, v2
	v_mov_b32_e32 v7, v2
	v_mov_b32_e32 v8, v2
	v_mov_b32_e32 v9, v2
	v_mov_b32_e32 v14, v2
	v_mov_b32_e32 v15, v2
	v_mov_b32_e32 v16, v2
	v_mov_b32_e32 v17, v2
	v_mov_b32_e32 v22, v2
	v_mov_b32_e32 v23, v2
	v_mov_b32_e32 v24, v2
	v_mov_b32_e32 v25, v2
	v_mov_b32_e32 v30, v2
	v_mov_b32_e32 v31, v2
	v_mov_b32_e32 v32, v2
	v_mov_b32_e32 v33, v2
	v_mov_b32_e32 v38, v2
	v_mov_b32_e32 v39, v2
	v_mov_b32_e32 v40, v2
	v_mov_b32_e32 v41, v2
	v_mov_b32_e32 v46, v2
	v_mov_b32_e32 v47, v2
	v_mov_b32_e32 v48, v2
	v_mov_b32_e32 v49, v2
	v_mov_b32_e32 v54, v2
	v_mov_b32_e32 v55, v2
	v_mov_b32_e32 v56, v2
	v_mov_b32_e32 v57, v2
	v_mov_b32_e32 v10, v2
	v_mov_b32_e32 v11, v2
	v_mov_b32_e32 v12, v2
	v_mov_b32_e32 v13, v2
	v_mov_b32_e32 v18, v2
	v_mov_b32_e32 v19, v2
	v_mov_b32_e32 v20, v2
	v_mov_b32_e32 v21, v2
	v_mov_b32_e32 v26, v2
	v_mov_b32_e32 v27, v2
	v_mov_b32_e32 v28, v2
	v_mov_b32_e32 v29, v2
	v_mov_b32_e32 v34, v2
	v_mov_b32_e32 v35, v2
	v_mov_b32_e32 v36, v2
	v_mov_b32_e32 v37, v2
	v_mov_b32_e32 v42, v2
	v_mov_b32_e32 v43, v2
	v_mov_b32_e32 v44, v2
	v_mov_b32_e32 v45, v2
	v_mov_b32_e32 v50, v2
	v_mov_b32_e32 v51, v2
	v_mov_b32_e32 v52, v2
	v_mov_b32_e32 v53, v2
	v_mov_b32_e32 v58, v2
	v_mov_b32_e32 v59, v2
	v_mov_b32_e32 v60, v2
	v_mov_b32_e32 v61, v2
	v_mov_b32_e32 v62, v2
	v_mov_b32_e32 v63, v2
	v_mov_b32_e32 v64, v2
	v_mov_b32_e32 v65, v2
	v_mov_b32_e32 v66, v2
	v_mov_b32_e32 v67, v2
	v_mov_b32_e32 v68, v2
	v_mov_b32_e32 v69, v2
	v_mov_b32_e32 v70, v2
	v_mov_b32_e32 v71, v2
	v_mov_b32_e32 v72, v2
	v_mov_b32_e32 v73, v2
	v_mov_b32_e32 v82, v2
	v_mov_b32_e32 v83, v2
	v_mov_b32_e32 v84, v2
	v_mov_b32_e32 v85, v2
	v_mov_b32_e32 v86, v2
	v_mov_b32_e32 v87, v2
	v_mov_b32_e32 v88, v2
	v_mov_b32_e32 v89, v2
	v_mov_b32_e32 v98, v2
	v_mov_b32_e32 v99, v2
	v_mov_b32_e32 v100, v2
	v_mov_b32_e32 v101, v2
	v_mov_b32_e32 v102, v2
	v_mov_b32_e32 v103, v2
	v_mov_b32_e32 v104, v2
	v_mov_b32_e32 v105, v2
	v_mov_b32_e32 v114, v2
	v_mov_b32_e32 v115, v2
	v_mov_b32_e32 v116, v2
	v_mov_b32_e32 v117, v2
	v_mov_b32_e32 v118, v2
	v_mov_b32_e32 v119, v2
	v_mov_b32_e32 v120, v2
	v_mov_b32_e32 v121, v2
	v_mov_b32_e32 v74, v2
	v_mov_b32_e32 v75, v2
	v_mov_b32_e32 v76, v2
	v_mov_b32_e32 v77, v2
	v_mov_b32_e32 v78, v2
	v_mov_b32_e32 v79, v2
	v_mov_b32_e32 v80, v2
	v_mov_b32_e32 v81, v2
	v_mov_b32_e32 v90, v2
	v_mov_b32_e32 v91, v2
	v_mov_b32_e32 v92, v2
	v_mov_b32_e32 v93, v2
	v_mov_b32_e32 v94, v2
	v_mov_b32_e32 v95, v2
	v_mov_b32_e32 v96, v2
	v_mov_b32_e32 v97, v2
	v_mov_b32_e32 v106, v2
	v_mov_b32_e32 v107, v2
	v_mov_b32_e32 v108, v2
	v_mov_b32_e32 v109, v2
	v_mov_b32_e32 v110, v2
	v_mov_b32_e32 v111, v2
	v_mov_b32_e32 v112, v2
	v_mov_b32_e32 v113, v2
	v_mov_b32_e32 v122, v2
	v_mov_b32_e32 v123, v2
	v_mov_b32_e32 v124, v2
	v_mov_b32_e32 v125, v2
	v_mov_b32_e32 v126, v2
	v_mov_b32_e32 v127, v2
	v_mov_b32_e32 v128, v2
	v_mov_b32_e32 v129, v2
	v_lshl_add_u32 v248, s38, 8, v143
	v_ashrrev_i32_e32 v249, 31, v248
	v_lshl_add_u64 v[248:249], v[248:249], 2, s[44:45]
	global_load_dword v240, v[248:249], off
	global_load_dword v241, v[248:249], off offset:64
	global_load_dword v242, v[248:249], off offset:128
	global_load_dword v243, v[248:249], off offset:192
	global_load_dword v244, v[248:249], off offset:512
	global_load_dword v245, v[248:249], off offset:576
	global_load_dword v246, v[248:249], off offset:640
	global_load_dword v247, v[248:249], off offset:704
	.p2alignl 6, 3212836864
